# P4b merge epilogue: Y row-group loads prefetched at epilogue start (groups 2-5) and 4 blocks ahead (6,7); counted vmcnt waits re-derived
# speedup vs baseline: 1.0211x; 1.0015x over previous
.LBB0_802:
	s_lshl_b32 s1, s0, 8
	s_and_b32 s26, s1, 0xfffffc00
	s_ashr_i32 s27, s26, 31
	s_and_b32 s19, s1, 0x300
	s_lshl_b64 s[30:31], s[26:27], 2
	v_or_b32_e32 v0, s19, v191
	s_add_u32 s30, s56, s30
	v_lshl_add_u32 v162, s28, 8, v190
	v_mov_b64_e32 v[18:19], s[12:13]
	s_movk_i32 s66, 0x1800
	s_addc_u32 s31, s57, s31
	v_lshlrev_b32_e32 v6, 2, v0
	v_mad_i64_i32 v[18:19], s[28:29], v162, s66, v[18:19]
	s_nop 15
	s_nop 3
	global_load_dwordx4 v[10:13], v6, s[30:31] offset:16
	global_load_dwordx4 v[14:17], v6, s[30:31]
	global_load_dwordx4 v[2:5], v6, s[30:31] offset:528
	s_nop 0
	global_load_dwordx4 v[6:9], v6, s[30:31] offset:512
	v_lshl_add_u64 v[18:19], s[26:27], 1, v[18:19]
	v_lshlrev_b32_e32 v0, 1, v0
	v_lshl_add_u64 v[18:19], v[18:19], 0, v[0:1]
	v_mov_b64_e32 v[240:241], v[18:19]
	global_load_dwordx4 v[30:33], v[18:19], off
	v_ashrrev_i32_e32 v163, 31, v162
	s_cmp_gt_u32 s0, 3
	s_cselect_b64 s[28:29], -1, 0
	v_lshlrev_b64 v[20:21], 11, v[162:163]
	v_readlane_b32 s68, v253, 41
	v_lshl_add_u64 v[178:179], s[10:11], 0, v[20:21]
	v_mov_b32_e32 v176, 0
	s_and_b64 vcc, exec, s[28:29]
	v_mov_b32_e32 v182, 0
	v_mov_b32_e32 v183, 0
	v_mov_b32_e32 v180, 0
	v_mov_b32_e32 v181, 0
	v_readlane_b32 s69, v253, 42
	v_readlane_b32 s67, v253, 52
	s_cbranch_vccz .LBB0_804
	v_lshl_add_u64 v[20:21], v[178:179], 0, v[0:1]
	global_load_dwordx2 v[182:183], v[20:21], off sc1
	global_load_dwordx2 v[180:181], v[20:21], off offset:8 sc1

.LBB0_810:
	s_mov_b32 s35, 0
	s_mov_b32 s34, 0x30000
	v_lshl_add_u64 v[246:247], v[240:241], 0, s[34:35]
	global_load_dwordx4 v[198:201], v[246:247], off
	global_load_dwordx4 v[202:205], v[246:247], off offset:256
	s_mov_b32 s34, 0x48000
	v_lshl_add_u64 v[246:247], v[240:241], 0, s[34:35]
	global_load_dwordx4 v[206:209], v[246:247], off
	global_load_dwordx4 v[216:219], v[246:247], off offset:256
	s_mov_b32 s34, 0xc0000
	v_lshl_add_u64 v[246:247], v[240:241], 0, s[34:35]
	global_load_dwordx4 v[224:227], v[246:247], off
	global_load_dwordx4 v[228:231], v[246:247], off offset:256
	s_mov_b32 s34, 0xd8000
	v_lshl_add_u64 v[246:247], v[240:241], 0, s[34:35]
	global_load_dwordx4 v[232:235], v[246:247], off
	global_load_dwordx4 v[236:239], v[246:247], off offset:256
	s_waitcnt vmcnt(14)
	v_add_f32_e32 v158, v158, v14
	v_add_f32_e32 v159, v159, v15
	v_mul_f32_e32 v158, 0xbfb8aa3b, v158
	v_mul_f32_e32 v159, 0xbfb8aa3b, v159
	v_exp_f32_e32 v158, v158
	v_exp_f32_e32 v159, v159
	s_waitcnt vmcnt(11)
	v_lshlrev_b32_e32 v194, 16, v30
	v_and_b32_e32 v195, 0xffff0000, v30
	v_add_f32_e32 v30, v160, v16
	v_mul_f32_e32 v30, 0xbfb8aa3b, v30
	v_add_f32_e32 v160, v161, v17
	v_exp_f32_e32 v30, v30
	v_mul_f32_e32 v160, 0xbfb8aa3b, v160
	v_exp_f32_e32 v161, v160
	v_add_f32_e32 v158, 1.0, v158
	v_add_f32_e32 v159, 1.0, v159
	v_rcp_f32_e32 v158, v158
	v_rcp_f32_e32 v159, v159
	v_add_f32_e32 v154, v154, v10
	v_add_f32_e32 v30, 1.0, v30
	v_mul_f32_e32 v154, 0xbfb8aa3b, v154
	v_rcp_f32_e32 v160, v30
	v_add_f32_e32 v30, 1.0, v161
	v_exp_f32_e32 v163, v154
	v_add_f32_e32 v154, v155, v11
	v_lshlrev_b32_e32 v196, 16, v182
	v_and_b32_e32 v197, 0xffff0000, v182
	v_rcp_f32_e32 v161, v30
	v_mul_f32_e32 v154, 0xbfb8aa3b, v154
	v_pk_fma_f32 v[158:159], v[158:159], v[194:195], v[196:197]
	v_exp_f32_e32 v194, v154
	v_lshlrev_b32_e32 v30, 16, v31
	v_and_b32_e32 v31, 0xffff0000, v31
	v_lshlrev_b32_e32 v182, 16, v183
	v_and_b32_e32 v183, 0xffff0000, v183
	v_pk_fma_f32 v[154:155], v[160:161], v[30:31], v[182:183]
	v_lshlrev_b32_e32 v160, 16, v32
	v_and_b32_e32 v161, 0xffff0000, v32
	v_add_f32_e32 v32, v156, v12
	v_add_f32_e32 v156, v157, v13
	v_add_f32_e32 v30, 1.0, v163
	v_add_f32_e32 v31, 1.0, v194
	v_mul_f32_e32 v32, 0xbfb8aa3b, v32
	v_mul_f32_e32 v156, 0xbfb8aa3b, v156
	v_rcp_f32_e32 v30, v30
	v_rcp_f32_e32 v31, v31
	v_exp_f32_e32 v32, v32
	v_exp_f32_e32 v163, v156
	v_lshlrev_b32_e32 v182, 16, v180
	v_and_b32_e32 v183, 0xffff0000, v180
	v_pk_fma_f32 v[156:157], v[30:31], v[160:161], v[182:183]
	v_add_f32_e32 v30, 1.0, v32
	v_add_f32_e32 v31, 1.0, v163
	v_rcp_f32_e32 v30, v30
	v_rcp_f32_e32 v31, v31
	v_add_f32_e32 v150, v150, v6
	v_add_f32_e32 v151, v151, v7
	v_lshlrev_b32_e32 v32, 16, v33
	v_and_b32_e32 v33, 0xffff0000, v33
	v_lshlrev_b32_e32 v160, 16, v181
	v_and_b32_e32 v161, 0xffff0000, v181
	v_mul_f32_e32 v150, 0xbfb8aa3b, v150
	v_mul_f32_e32 v151, 0xbfb8aa3b, v151
	v_pk_fma_f32 v[160:161], v[30:31], v[32:33], v[160:161]
	v_exp_f32_e32 v150, v150
	v_exp_f32_e32 v151, v151
	v_cvt_pk_bf16_f32 v30, v158, v159
	v_cvt_pk_bf16_f32 v31, v154, v155
	v_cvt_pk_bf16_f32 v32, v156, v157
	v_cvt_pk_bf16_f32 v33, v160, v161
	v_lshl_add_u64 v[154:155], v[178:179], 0, v[0:1]
	global_store_dwordx4 v[154:155], v[30:33], off
	v_add_f32_e32 v146, v146, v2
	v_add_f32_e32 v147, v147, v3
	s_waitcnt vmcnt(11)
	v_lshlrev_b32_e32 v32, 16, v22
	v_and_b32_e32 v33, 0xffff0000, v22
	v_add_f32_e32 v22, v152, v8
	v_mul_f32_e32 v22, 0xbfb8aa3b, v22
	v_add_f32_e32 v152, v153, v9
	v_add_f32_e32 v30, 1.0, v150
	v_add_f32_e32 v31, 1.0, v151
	v_exp_f32_e32 v22, v22
	v_mul_f32_e32 v152, 0xbfb8aa3b, v152
	v_rcp_f32_e32 v30, v30
	v_rcp_f32_e32 v31, v31
	v_exp_f32_e32 v152, v152
	v_lshlrev_b32_e32 v150, 16, v176
	v_and_b32_e32 v151, 0xffff0000, v176
	v_add_f32_e32 v22, 1.0, v22
	v_pk_fma_f32 v[30:31], v[30:31], v[32:33], v[150:151]
	v_rcp_f32_e32 v32, v22
	v_add_f32_e32 v22, 1.0, v152
	v_mul_f32_e32 v146, 0xbfb8aa3b, v146
	v_mul_f32_e32 v147, 0xbfb8aa3b, v147
	v_rcp_f32_e32 v33, v22
	v_exp_f32_e32 v146, v146
	v_exp_f32_e32 v147, v147
	v_lshlrev_b32_e32 v22, 16, v23
	v_and_b32_e32 v23, 0xffff0000, v23
	v_lshlrev_b32_e32 v150, 16, v177
	v_and_b32_e32 v151, 0xffff0000, v177
	v_pk_fma_f32 v[32:33], v[32:33], v[22:23], v[150:151]
	v_add_f32_e32 v22, 1.0, v146
	v_add_f32_e32 v23, 1.0, v147
	v_lshlrev_b32_e32 v146, 16, v24
	v_and_b32_e32 v147, 0xffff0000, v24
	v_add_f32_e32 v24, v148, v4
	v_add_f32_e32 v148, v149, v5
	v_mul_f32_e32 v24, 0xbfb8aa3b, v24
	v_mul_f32_e32 v148, 0xbfb8aa3b, v148
	v_rcp_f32_e32 v22, v22
	v_rcp_f32_e32 v23, v23
	v_exp_f32_e32 v24, v24
	v_exp_f32_e32 v148, v148
	v_lshlrev_b32_e32 v150, 16, v174
	v_and_b32_e32 v151, 0xffff0000, v174
	v_pk_fma_f32 v[146:147], v[22:23], v[146:147], v[150:151]
	v_add_f32_e32 v22, 1.0, v24
	v_add_f32_e32 v23, 1.0, v148
	v_rcp_f32_e32 v22, v22
	v_rcp_f32_e32 v23, v23
	v_lshlrev_b32_e32 v24, 16, v25
	v_and_b32_e32 v25, 0xffff0000, v25
	v_lshlrev_b32_e32 v148, 16, v175
	v_and_b32_e32 v149, 0xffff0000, v175
	v_pk_fma_f32 v[148:149], v[22:23], v[24:25], v[148:149]
	v_cvt_pk_bf16_f32 v22, v30, v31
	v_cvt_pk_bf16_f32 v23, v32, v33
	v_cvt_pk_bf16_f32 v24, v146, v147
	v_cvt_pk_bf16_f32 v25, v148, v149
	global_store_dwordx4 v[154:155], v[22:25], off offset:256
	v_mov_b32_e32 v148, 0
	s_and_b64 vcc, exec, s[0:1]
	v_or_b32_e32 v24, 32, v162
	v_mov_b64_e32 v[22:23], s[12:13]
	v_mad_i64_i32 v[22:23], s[28:29], v24, s66, v[22:23]
	v_lshl_add_u64 v[22:23], s[26:27], 1, v[22:23]
	v_lshl_add_u64 v[22:23], v[22:23], 0, v[0:1]
	v_ashrrev_i32_e32 v25, 31, v24
	v_lshlrev_b64 v[24:25], 11, v[24:25]
	v_lshl_add_u64 v[150:151], s[10:11], 0, v[24:25]
	v_mov_b32_e32 v154, 0
	v_mov_b32_e32 v155, 0
	v_mov_b32_e32 v152, 0
	v_mov_b32_e32 v153, 0
	s_cbranch_vccnz .LBB0_812
	v_lshl_add_u64 v[24:25], v[150:151], 0, v[0:1]
	global_load_dwordx2 v[154:155], v[24:25], off sc1
	global_load_dwordx2 v[152:153], v[24:25], off offset:8 sc1
.LBB0_812:
	s_nop 0
	s_and_b64 vcc, exec, s[0:1]
	v_mov_b32_e32 v149, 0
	v_mov_b32_e32 v146, 0
	v_mov_b32_e32 v147, 0
	s_cbranch_vccnz .LBB0_814
	v_lshl_add_u64 v[146:147], v[150:151], 0, v[0:1]
	global_load_dwordx2 v[148:149], v[146:147], off offset:256 sc1
	s_nop 0
	global_load_dwordx2 v[146:147], v[146:147], off offset:264 sc1
.LBB0_814:
	v_add_f32_e32 v142, v142, v14
	v_add_f32_e32 v143, v143, v15
	v_mul_f32_e32 v142, 0xbfb8aa3b, v142
	v_mul_f32_e32 v143, 0xbfb8aa3b, v143
	v_exp_f32_e32 v142, v142
	v_exp_f32_e32 v143, v143
	s_waitcnt vmcnt(11)
	v_lshlrev_b32_e32 v156, 16, v26
	v_and_b32_e32 v157, 0xffff0000, v26
	v_add_f32_e32 v26, v144, v16
	v_mul_f32_e32 v26, 0xbfb8aa3b, v26
	v_add_f32_e32 v144, v145, v17
	v_add_f32_e32 v142, 1.0, v142
	v_add_f32_e32 v143, 1.0, v143
	v_exp_f32_e32 v26, v26
	v_mul_f32_e32 v144, 0xbfb8aa3b, v144
	v_rcp_f32_e32 v142, v142
	v_rcp_f32_e32 v143, v143
	v_exp_f32_e32 v145, v144
	v_add_f32_e32 v138, v138, v10
	v_lshlrev_b32_e32 v158, 16, v172
	v_and_b32_e32 v159, 0xffff0000, v172
	v_add_f32_e32 v26, 1.0, v26
	v_mul_f32_e32 v138, 0xbfb8aa3b, v138
	v_pk_fma_f32 v[142:143], v[142:143], v[156:157], v[158:159]
	v_rcp_f32_e32 v144, v26
	v_add_f32_e32 v26, 1.0, v145
	v_exp_f32_e32 v158, v138
	v_add_f32_e32 v138, v139, v11
	v_rcp_f32_e32 v145, v26
	v_mul_f32_e32 v138, 0xbfb8aa3b, v138
	v_exp_f32_e32 v159, v138
	v_lshlrev_b32_e32 v26, 16, v27
	v_and_b32_e32 v27, 0xffff0000, v27
	v_lshlrev_b32_e32 v156, 16, v173
	v_and_b32_e32 v157, 0xffff0000, v173
	v_pk_fma_f32 v[138:139], v[144:145], v[26:27], v[156:157]
	v_lshlrev_b32_e32 v144, 16, v28
	v_and_b32_e32 v145, 0xffff0000, v28
	v_add_f32_e32 v28, v140, v12
	v_add_f32_e32 v140, v141, v13
	v_add_f32_e32 v26, 1.0, v158
	v_add_f32_e32 v27, 1.0, v159
	v_mul_f32_e32 v28, 0xbfb8aa3b, v28
	v_mul_f32_e32 v140, 0xbfb8aa3b, v140
	v_rcp_f32_e32 v26, v26
	v_rcp_f32_e32 v27, v27
	v_exp_f32_e32 v28, v28
	v_exp_f32_e32 v158, v140
	v_lshlrev_b32_e32 v156, 16, v170
	v_and_b32_e32 v157, 0xffff0000, v170
	v_pk_fma_f32 v[140:141], v[26:27], v[144:145], v[156:157]
	v_add_f32_e32 v26, 1.0, v28
	v_add_f32_e32 v27, 1.0, v158
	v_rcp_f32_e32 v26, v26
	v_rcp_f32_e32 v27, v27
	v_add_f32_e32 v134, v134, v6
	v_add_f32_e32 v135, v135, v7
	v_lshlrev_b32_e32 v28, 16, v29
	v_and_b32_e32 v29, 0xffff0000, v29
	v_lshlrev_b32_e32 v144, 16, v171
	v_and_b32_e32 v145, 0xffff0000, v171
	v_mul_f32_e32 v134, 0xbfb8aa3b, v134
	v_mul_f32_e32 v135, 0xbfb8aa3b, v135
	v_pk_fma_f32 v[144:145], v[26:27], v[28:29], v[144:145]
	v_exp_f32_e32 v134, v134
	v_exp_f32_e32 v135, v135
	v_cvt_pk_bf16_f32 v26, v142, v143
	v_cvt_pk_bf16_f32 v27, v138, v139
	v_cvt_pk_bf16_f32 v28, v140, v141
	v_cvt_pk_bf16_f32 v29, v144, v145
	v_lshl_add_u64 v[138:139], v[168:169], 0, v[0:1]
	global_store_dwordx4 v[138:139], v[26:29], off
	v_add_f32_e32 v130, v130, v2
	v_add_f32_e32 v131, v131, v3
	s_waitcnt vmcnt(11)
	v_lshlrev_b32_e32 v28, 16, v18
	v_and_b32_e32 v29, 0xffff0000, v18
	v_add_f32_e32 v18, v136, v8
	v_mul_f32_e32 v18, 0xbfb8aa3b, v18
	v_add_f32_e32 v136, v137, v9
	v_add_f32_e32 v26, 1.0, v134
	v_add_f32_e32 v27, 1.0, v135
	v_exp_f32_e32 v18, v18
	v_mul_f32_e32 v136, 0xbfb8aa3b, v136
	v_rcp_f32_e32 v26, v26
	v_rcp_f32_e32 v27, v27
	v_exp_f32_e32 v136, v136
	v_lshlrev_b32_e32 v134, 16, v166
	v_and_b32_e32 v135, 0xffff0000, v166
	v_add_f32_e32 v18, 1.0, v18
	v_pk_fma_f32 v[26:27], v[26:27], v[28:29], v[134:135]
	v_rcp_f32_e32 v28, v18
	v_add_f32_e32 v18, 1.0, v136
	v_mul_f32_e32 v130, 0xbfb8aa3b, v130
	v_mul_f32_e32 v131, 0xbfb8aa3b, v131
	v_rcp_f32_e32 v29, v18
	v_exp_f32_e32 v130, v130
	v_exp_f32_e32 v131, v131
	v_lshlrev_b32_e32 v18, 16, v19
	v_and_b32_e32 v19, 0xffff0000, v19
	v_lshlrev_b32_e32 v134, 16, v167
	v_and_b32_e32 v135, 0xffff0000, v167
	v_pk_fma_f32 v[28:29], v[28:29], v[18:19], v[134:135]
	v_add_f32_e32 v18, 1.0, v130
	v_add_f32_e32 v19, 1.0, v131
	v_lshlrev_b32_e32 v130, 16, v20
	v_and_b32_e32 v131, 0xffff0000, v20
	v_add_f32_e32 v20, v132, v4
	v_add_f32_e32 v132, v133, v5
	v_mul_f32_e32 v20, 0xbfb8aa3b, v20
	v_mul_f32_e32 v132, 0xbfb8aa3b, v132
	v_rcp_f32_e32 v18, v18
	v_rcp_f32_e32 v19, v19
	v_exp_f32_e32 v20, v20
	v_exp_f32_e32 v132, v132
	v_lshlrev_b32_e32 v134, 16, v164
	v_and_b32_e32 v135, 0xffff0000, v164
	v_pk_fma_f32 v[130:131], v[18:19], v[130:131], v[134:135]
	v_add_f32_e32 v18, 1.0, v20
	v_add_f32_e32 v19, 1.0, v132
	v_rcp_f32_e32 v18, v18
	v_rcp_f32_e32 v19, v19
	v_lshlrev_b32_e32 v20, 16, v21
	v_and_b32_e32 v21, 0xffff0000, v21
	v_lshlrev_b32_e32 v132, 16, v165
	v_and_b32_e32 v133, 0xffff0000, v165
	v_pk_fma_f32 v[132:133], v[18:19], v[20:21], v[132:133]
	v_cvt_pk_bf16_f32 v18, v26, v27
	v_cvt_pk_bf16_f32 v19, v28, v29
	v_cvt_pk_bf16_f32 v20, v130, v131
	v_cvt_pk_bf16_f32 v21, v132, v133
	global_store_dwordx4 v[138:139], v[18:21], off offset:256
	v_mov_b32_e32 v132, 0
	s_and_b64 vcc, exec, s[0:1]
	v_or_b32_e32 v20, 48, v162
	v_mov_b64_e32 v[18:19], s[12:13]
	v_mad_i64_i32 v[18:19], s[28:29], v20, s66, v[18:19]
	v_lshl_add_u64 v[18:19], s[26:27], 1, v[18:19]
	v_lshl_add_u64 v[18:19], v[18:19], 0, v[0:1]
	v_ashrrev_i32_e32 v21, 31, v20
	v_lshlrev_b64 v[20:21], 11, v[20:21]
	v_lshl_add_u64 v[134:135], s[10:11], 0, v[20:21]
	v_mov_b32_e32 v138, 0
	v_mov_b32_e32 v139, 0
	v_mov_b32_e32 v136, 0
	v_mov_b32_e32 v137, 0
	s_cbranch_vccnz .LBB0_816
	v_lshl_add_u64 v[20:21], v[134:135], 0, v[0:1]
	global_load_dwordx2 v[138:139], v[20:21], off sc1
	global_load_dwordx2 v[136:137], v[20:21], off offset:8 sc1
.LBB0_816:
	s_nop 0
	s_and_b64 vcc, exec, s[0:1]
	v_mov_b32_e32 v133, 0
	v_mov_b32_e32 v130, 0
	v_mov_b32_e32 v131, 0
	s_cbranch_vccnz .LBB0_818
	v_lshl_add_u64 v[130:131], v[134:135], 0, v[0:1]
	global_load_dwordx2 v[132:133], v[130:131], off offset:256 sc1
	s_nop 0
	global_load_dwordx2 v[130:131], v[130:131], off offset:264 sc1
.LBB0_818:
	v_add_f32_e32 v126, v126, v14
	v_add_f32_e32 v127, v127, v15
	v_mul_f32_e32 v126, 0xbfb8aa3b, v126
	v_mul_f32_e32 v127, 0xbfb8aa3b, v127
	v_exp_f32_e32 v126, v126
	v_exp_f32_e32 v127, v127
	s_waitcnt vmcnt(8)
	v_lshlrev_b32_e32 v140, 16, v198
	v_and_b32_e32 v141, 0xffff0000, v198
	v_add_f32_e32 v198, v128, v16
	v_mul_f32_e32 v198, 0xbfb8aa3b, v198
	v_add_f32_e32 v128, v129, v17
	v_add_f32_e32 v126, 1.0, v126
	v_add_f32_e32 v127, 1.0, v127
	v_exp_f32_e32 v198, v198
	v_mul_f32_e32 v128, 0xbfb8aa3b, v128
	v_rcp_f32_e32 v126, v126
	v_rcp_f32_e32 v127, v127
	v_exp_f32_e32 v129, v128
	v_add_f32_e32 v122, v122, v10
	v_lshlrev_b32_e32 v142, 16, v154
	v_and_b32_e32 v143, 0xffff0000, v154
	v_add_f32_e32 v198, 1.0, v198
	v_mul_f32_e32 v122, 0xbfb8aa3b, v122
	v_pk_fma_f32 v[126:127], v[126:127], v[140:141], v[142:143]
	v_rcp_f32_e32 v128, v198
	v_add_f32_e32 v198, 1.0, v129
	v_exp_f32_e32 v142, v122
	v_add_f32_e32 v122, v123, v11
	v_rcp_f32_e32 v129, v198
	v_mul_f32_e32 v122, 0xbfb8aa3b, v122
	v_exp_f32_e32 v143, v122
	v_lshlrev_b32_e32 v198, 16, v199
	v_and_b32_e32 v199, 0xffff0000, v199
	v_lshlrev_b32_e32 v140, 16, v155
	v_and_b32_e32 v141, 0xffff0000, v155
	v_pk_fma_f32 v[122:123], v[128:129], v[198:199], v[140:141]
	v_lshlrev_b32_e32 v128, 16, v200
	v_and_b32_e32 v129, 0xffff0000, v200
	v_add_f32_e32 v200, v124, v12
	v_add_f32_e32 v124, v125, v13
	v_add_f32_e32 v198, 1.0, v142
	v_add_f32_e32 v199, 1.0, v143
	v_mul_f32_e32 v200, 0xbfb8aa3b, v200
	v_mul_f32_e32 v124, 0xbfb8aa3b, v124
	v_rcp_f32_e32 v198, v198
	v_rcp_f32_e32 v199, v199
	v_exp_f32_e32 v200, v200
	v_exp_f32_e32 v142, v124
	v_lshlrev_b32_e32 v140, 16, v152
	v_and_b32_e32 v141, 0xffff0000, v152
	v_pk_fma_f32 v[124:125], v[198:199], v[128:129], v[140:141]
	v_add_f32_e32 v198, 1.0, v200
	v_add_f32_e32 v199, 1.0, v142
	v_rcp_f32_e32 v198, v198
	v_rcp_f32_e32 v199, v199
	v_add_f32_e32 v118, v118, v6
	v_add_f32_e32 v119, v119, v7
	v_lshlrev_b32_e32 v200, 16, v201
	v_and_b32_e32 v201, 0xffff0000, v201
	v_lshlrev_b32_e32 v128, 16, v153
	v_and_b32_e32 v129, 0xffff0000, v153
	v_mul_f32_e32 v118, 0xbfb8aa3b, v118
	v_mul_f32_e32 v119, 0xbfb8aa3b, v119
	v_pk_fma_f32 v[128:129], v[198:199], v[200:201], v[128:129]
	v_exp_f32_e32 v118, v118
	v_exp_f32_e32 v119, v119
	v_cvt_pk_bf16_f32 v198, v126, v127
	v_cvt_pk_bf16_f32 v199, v122, v123
	v_cvt_pk_bf16_f32 v200, v124, v125
	v_cvt_pk_bf16_f32 v201, v128, v129
	v_lshl_add_u64 v[122:123], v[150:151], 0, v[0:1]
	global_store_dwordx4 v[122:123], v[198:201], off
	v_add_f32_e32 v114, v114, v2
	v_add_f32_e32 v115, v115, v3
	s_waitcnt vmcnt(7)
	v_lshlrev_b32_e32 v200, 16, v202
	v_and_b32_e32 v201, 0xffff0000, v202
	v_add_f32_e32 v202, v120, v8
	v_mul_f32_e32 v202, 0xbfb8aa3b, v202
	v_add_f32_e32 v120, v121, v9
	v_add_f32_e32 v198, 1.0, v118
	v_add_f32_e32 v199, 1.0, v119
	v_exp_f32_e32 v202, v202
	v_mul_f32_e32 v120, 0xbfb8aa3b, v120
	v_rcp_f32_e32 v198, v198
	v_rcp_f32_e32 v199, v199
	v_exp_f32_e32 v120, v120
	v_lshlrev_b32_e32 v118, 16, v148
	v_and_b32_e32 v119, 0xffff0000, v148
	v_add_f32_e32 v202, 1.0, v202
	v_pk_fma_f32 v[198:199], v[198:199], v[200:201], v[118:119]
	v_rcp_f32_e32 v200, v202
	v_add_f32_e32 v202, 1.0, v120
	v_mul_f32_e32 v114, 0xbfb8aa3b, v114
	v_mul_f32_e32 v115, 0xbfb8aa3b, v115
	v_rcp_f32_e32 v201, v202
	v_exp_f32_e32 v114, v114
	v_exp_f32_e32 v115, v115
	v_lshlrev_b32_e32 v202, 16, v203
	v_and_b32_e32 v203, 0xffff0000, v203
	v_lshlrev_b32_e32 v118, 16, v149
	v_and_b32_e32 v119, 0xffff0000, v149
	v_pk_fma_f32 v[200:201], v[200:201], v[202:203], v[118:119]
	v_add_f32_e32 v202, 1.0, v114
	v_add_f32_e32 v203, 1.0, v115
	v_lshlrev_b32_e32 v114, 16, v204
	v_and_b32_e32 v115, 0xffff0000, v204
	v_add_f32_e32 v204, v116, v4
	v_add_f32_e32 v116, v117, v5
	v_mul_f32_e32 v204, 0xbfb8aa3b, v204
	v_mul_f32_e32 v116, 0xbfb8aa3b, v116
	v_rcp_f32_e32 v202, v202
	v_rcp_f32_e32 v203, v203
	v_exp_f32_e32 v204, v204
	v_exp_f32_e32 v116, v116
	v_lshlrev_b32_e32 v118, 16, v146
	v_and_b32_e32 v119, 0xffff0000, v146
	v_pk_fma_f32 v[114:115], v[202:203], v[114:115], v[118:119]
	v_add_f32_e32 v202, 1.0, v204
	v_add_f32_e32 v203, 1.0, v116
	v_rcp_f32_e32 v202, v202
	v_rcp_f32_e32 v203, v203
	v_lshlrev_b32_e32 v204, 16, v205
	v_and_b32_e32 v205, 0xffff0000, v205
	v_lshlrev_b32_e32 v116, 16, v147
	v_and_b32_e32 v117, 0xffff0000, v147
	v_pk_fma_f32 v[116:117], v[202:203], v[204:205], v[116:117]
	v_cvt_pk_bf16_f32 v202, v198, v199
	v_cvt_pk_bf16_f32 v203, v200, v201
	v_cvt_pk_bf16_f32 v204, v114, v115
	v_cvt_pk_bf16_f32 v205, v116, v117
	global_store_dwordx4 v[122:123], v[202:205], off offset:256
	v_add_u32_e32 v114, 0x80, v162
	v_ashrrev_i32_e32 v115, 31, v114
	v_mov_b64_e32 v[22:23], s[12:13]
	v_mad_i64_i32 v[22:23], s[28:29], v114, s66, v[22:23]
	v_lshl_add_u64 v[22:23], s[26:27], 1, v[22:23]
	v_lshl_add_u64 v[22:23], v[22:23], 0, v[0:1]
	s_mov_b32 s34, 0xf0000
	v_lshl_add_u64 v[246:247], v[240:241], 0, s[34:35]
	global_load_dwordx4 v[198:201], v[246:247], off
	v_lshlrev_b64 v[24:25], 11, v[114:115]
	v_lshl_add_u64 v[120:121], s[10:11], 0, v[24:25]
	v_mov_b32_e32 v118, 0
	s_and_b64 vcc, exec, s[0:1]
	v_mov_b32_e32 v124, 0
	v_mov_b32_e32 v125, 0
	v_mov_b32_e32 v122, 0
	v_mov_b32_e32 v123, 0
	s_cbranch_vccnz .LBB0_820
	v_lshl_add_u64 v[24:25], v[120:121], 0, v[0:1]
	global_load_dwordx2 v[124:125], v[24:25], off sc1
	global_load_dwordx2 v[122:123], v[24:25], off offset:8 sc1
.LBB0_820:
	s_nop 0
	global_load_dwordx4 v[202:205], v[246:247], off offset:256
	s_and_b64 vcc, exec, s[0:1]
	v_mov_b32_e32 v119, 0
	v_mov_b32_e32 v116, 0
	v_mov_b32_e32 v117, 0
	s_cbranch_vccnz .LBB0_822
	v_lshl_add_u64 v[116:117], v[120:121], 0, v[0:1]
	global_load_dwordx2 v[118:119], v[116:117], off offset:256 sc1
	s_nop 0
	global_load_dwordx2 v[116:117], v[116:117], off offset:264 sc1
.LBB0_822:
	v_add_f32_e32 v110, v110, v14
	v_add_f32_e32 v111, v111, v15
	v_mul_f32_e32 v110, 0xbfb8aa3b, v110
	v_mul_f32_e32 v111, 0xbfb8aa3b, v111
	v_exp_f32_e32 v110, v110
	v_exp_f32_e32 v111, v111
	s_waitcnt vmcnt(10)
	v_lshlrev_b32_e32 v126, 16, v206
	v_and_b32_e32 v127, 0xffff0000, v206
	v_add_f32_e32 v206, v112, v16
	v_mul_f32_e32 v206, 0xbfb8aa3b, v206
	v_add_f32_e32 v112, v113, v17
	v_exp_f32_e32 v206, v206
	v_mul_f32_e32 v112, 0xbfb8aa3b, v112
	v_exp_f32_e32 v113, v112
	v_add_f32_e32 v110, 1.0, v110
	v_add_f32_e32 v111, 1.0, v111
	v_rcp_f32_e32 v110, v110
	v_rcp_f32_e32 v111, v111
	v_add_f32_e32 v106, v106, v10
	v_add_f32_e32 v206, 1.0, v206
	v_mul_f32_e32 v106, 0xbfb8aa3b, v106
	v_rcp_f32_e32 v112, v206
	v_add_f32_e32 v206, 1.0, v113
	v_exp_f32_e32 v115, v106
	v_add_f32_e32 v106, v107, v11
	v_lshlrev_b32_e32 v128, 16, v138
	v_and_b32_e32 v129, 0xffff0000, v138
	v_rcp_f32_e32 v113, v206
	v_mul_f32_e32 v106, 0xbfb8aa3b, v106
	v_pk_fma_f32 v[110:111], v[110:111], v[126:127], v[128:129]
	v_exp_f32_e32 v128, v106
	v_lshlrev_b32_e32 v206, 16, v207
	v_and_b32_e32 v207, 0xffff0000, v207
	v_lshlrev_b32_e32 v126, 16, v139
	v_and_b32_e32 v127, 0xffff0000, v139
	v_pk_fma_f32 v[106:107], v[112:113], v[206:207], v[126:127]
	v_lshlrev_b32_e32 v112, 16, v208
	v_and_b32_e32 v113, 0xffff0000, v208
	v_add_f32_e32 v208, v108, v12
	v_add_f32_e32 v108, v109, v13
	v_add_f32_e32 v206, 1.0, v115
	v_add_f32_e32 v207, 1.0, v128
	v_mul_f32_e32 v208, 0xbfb8aa3b, v208
	v_mul_f32_e32 v108, 0xbfb8aa3b, v108
	v_rcp_f32_e32 v206, v206
	v_rcp_f32_e32 v207, v207
	v_exp_f32_e32 v208, v208
	v_exp_f32_e32 v115, v108
	v_lshlrev_b32_e32 v126, 16, v136
	v_and_b32_e32 v127, 0xffff0000, v136
	v_pk_fma_f32 v[108:109], v[206:207], v[112:113], v[126:127]
	v_add_f32_e32 v206, 1.0, v208
	v_add_f32_e32 v207, 1.0, v115
	v_rcp_f32_e32 v206, v206
	v_rcp_f32_e32 v207, v207
	v_add_f32_e32 v102, v102, v6
	v_add_f32_e32 v103, v103, v7
	v_lshlrev_b32_e32 v208, 16, v209
	v_and_b32_e32 v209, 0xffff0000, v209
	v_lshlrev_b32_e32 v112, 16, v137
	v_and_b32_e32 v113, 0xffff0000, v137
	v_mul_f32_e32 v102, 0xbfb8aa3b, v102
	v_mul_f32_e32 v103, 0xbfb8aa3b, v103
	v_pk_fma_f32 v[112:113], v[206:207], v[208:209], v[112:113]
	v_exp_f32_e32 v102, v102
	v_exp_f32_e32 v103, v103
	v_cvt_pk_bf16_f32 v206, v110, v111
	v_cvt_pk_bf16_f32 v207, v106, v107
	v_cvt_pk_bf16_f32 v208, v108, v109
	v_cvt_pk_bf16_f32 v209, v112, v113
	v_lshl_add_u64 v[106:107], v[134:135], 0, v[0:1]
	global_store_dwordx4 v[106:107], v[206:209], off
	v_add_f32_e32 v98, v98, v2
	v_add_f32_e32 v99, v99, v3
	s_waitcnt vmcnt(9)
	v_lshlrev_b32_e32 v208, 16, v216
	v_and_b32_e32 v209, 0xffff0000, v216
	v_add_f32_e32 v216, v104, v8
	v_mul_f32_e32 v216, 0xbfb8aa3b, v216
	v_add_f32_e32 v104, v105, v9
	v_add_f32_e32 v206, 1.0, v102
	v_add_f32_e32 v207, 1.0, v103
	v_exp_f32_e32 v216, v216
	v_mul_f32_e32 v104, 0xbfb8aa3b, v104
	v_rcp_f32_e32 v206, v206
	v_rcp_f32_e32 v207, v207
	v_exp_f32_e32 v104, v104
	v_lshlrev_b32_e32 v102, 16, v132
	v_and_b32_e32 v103, 0xffff0000, v132
	v_add_f32_e32 v216, 1.0, v216
	v_pk_fma_f32 v[206:207], v[206:207], v[208:209], v[102:103]
	v_rcp_f32_e32 v208, v216
	v_add_f32_e32 v216, 1.0, v104
	v_mul_f32_e32 v98, 0xbfb8aa3b, v98
	v_mul_f32_e32 v99, 0xbfb8aa3b, v99
	v_rcp_f32_e32 v209, v216
	v_exp_f32_e32 v98, v98
	v_exp_f32_e32 v99, v99
	v_lshlrev_b32_e32 v216, 16, v217
	v_and_b32_e32 v217, 0xffff0000, v217
	v_lshlrev_b32_e32 v102, 16, v133
	v_and_b32_e32 v103, 0xffff0000, v133
	v_pk_fma_f32 v[208:209], v[208:209], v[216:217], v[102:103]
	v_add_f32_e32 v216, 1.0, v98
	v_add_f32_e32 v217, 1.0, v99
	v_lshlrev_b32_e32 v98, 16, v218
	v_and_b32_e32 v99, 0xffff0000, v218
	v_add_f32_e32 v218, v100, v4
	v_add_f32_e32 v100, v101, v5
	v_mul_f32_e32 v218, 0xbfb8aa3b, v218
	v_mul_f32_e32 v100, 0xbfb8aa3b, v100
	v_rcp_f32_e32 v216, v216
	v_rcp_f32_e32 v217, v217
	v_exp_f32_e32 v218, v218
	v_exp_f32_e32 v100, v100
	v_lshlrev_b32_e32 v102, 16, v130
	v_and_b32_e32 v103, 0xffff0000, v130
	v_pk_fma_f32 v[98:99], v[216:217], v[98:99], v[102:103]
	v_add_f32_e32 v216, 1.0, v218
	v_add_f32_e32 v217, 1.0, v100
	v_rcp_f32_e32 v216, v216
	v_rcp_f32_e32 v217, v217
	v_lshlrev_b32_e32 v218, 16, v219
	v_and_b32_e32 v219, 0xffff0000, v219
	v_lshlrev_b32_e32 v100, 16, v131
	v_and_b32_e32 v101, 0xffff0000, v131
	v_pk_fma_f32 v[100:101], v[216:217], v[218:219], v[100:101]
	v_cvt_pk_bf16_f32 v216, v206, v207
	v_cvt_pk_bf16_f32 v217, v208, v209
	v_cvt_pk_bf16_f32 v218, v98, v99
	v_cvt_pk_bf16_f32 v219, v100, v101
	global_store_dwordx4 v[106:107], v[216:219], off offset:256
	v_mov_b32_e32 v100, 0
	s_and_b64 vcc, exec, s[0:1]
	v_or_b32_e32 v20, 16, v114
	v_mov_b64_e32 v[18:19], s[12:13]
	v_mad_i64_i32 v[18:19], s[28:29], v20, s66, v[18:19]
	v_lshl_add_u64 v[18:19], s[26:27], 1, v[18:19]
	v_lshl_add_u64 v[18:19], v[18:19], 0, v[0:1]
	s_mov_b32 s34, 0x108000
	v_lshl_add_u64 v[246:247], v[240:241], 0, s[34:35]
	global_load_dwordx4 v[206:209], v[246:247], off
	v_ashrrev_i32_e32 v21, 31, v20
	v_lshlrev_b64 v[20:21], 11, v[20:21]
	v_lshl_add_u64 v[102:103], s[10:11], 0, v[20:21]
	v_mov_b32_e32 v106, 0
	v_mov_b32_e32 v107, 0
	v_mov_b32_e32 v104, 0
	v_mov_b32_e32 v105, 0
	s_cbranch_vccnz .LBB0_824
	v_lshl_add_u64 v[20:21], v[102:103], 0, v[0:1]
	global_load_dwordx2 v[106:107], v[20:21], off sc1
	global_load_dwordx2 v[104:105], v[20:21], off offset:8 sc1
.LBB0_824:
	s_nop 0
	global_load_dwordx4 v[216:219], v[246:247], off offset:256
	s_and_b64 vcc, exec, s[0:1]
	v_mov_b32_e32 v101, 0
	v_mov_b32_e32 v98, 0
	v_mov_b32_e32 v99, 0
	s_cbranch_vccnz .LBB0_826
	v_lshl_add_u64 v[98:99], v[102:103], 0, v[0:1]
	global_load_dwordx2 v[100:101], v[98:99], off offset:256 sc1
	s_nop 0
	global_load_dwordx2 v[98:99], v[98:99], off offset:264 sc1
.LBB0_826:
	v_add_f32_e32 v94, v94, v14
	v_add_f32_e32 v95, v95, v15
	v_mul_f32_e32 v94, 0xbfb8aa3b, v94
	v_mul_f32_e32 v95, 0xbfb8aa3b, v95
	v_exp_f32_e32 v94, v94
	v_exp_f32_e32 v95, v95
	s_waitcnt vmcnt(11)
	v_lshlrev_b32_e32 v108, 16, v224
	v_and_b32_e32 v109, 0xffff0000, v224
	v_add_f32_e32 v224, v96, v16
	v_mul_f32_e32 v224, 0xbfb8aa3b, v224
	v_add_f32_e32 v96, v97, v17
	v_add_f32_e32 v94, 1.0, v94
	v_add_f32_e32 v95, 1.0, v95
	v_exp_f32_e32 v224, v224
	v_mul_f32_e32 v96, 0xbfb8aa3b, v96
	v_rcp_f32_e32 v94, v94
	v_rcp_f32_e32 v95, v95
	v_exp_f32_e32 v97, v96
	v_add_f32_e32 v90, v90, v10
	v_lshlrev_b32_e32 v110, 16, v124
	v_and_b32_e32 v111, 0xffff0000, v124
	v_add_f32_e32 v224, 1.0, v224
	v_mul_f32_e32 v90, 0xbfb8aa3b, v90
	v_pk_fma_f32 v[94:95], v[94:95], v[108:109], v[110:111]
	v_rcp_f32_e32 v96, v224
	v_add_f32_e32 v224, 1.0, v97
	v_exp_f32_e32 v110, v90
	v_add_f32_e32 v90, v91, v11
	v_rcp_f32_e32 v97, v224
	v_mul_f32_e32 v90, 0xbfb8aa3b, v90
	v_exp_f32_e32 v111, v90
	v_lshlrev_b32_e32 v224, 16, v225
	v_and_b32_e32 v225, 0xffff0000, v225
	v_lshlrev_b32_e32 v108, 16, v125
	v_and_b32_e32 v109, 0xffff0000, v125
	v_pk_fma_f32 v[90:91], v[96:97], v[224:225], v[108:109]
	v_lshlrev_b32_e32 v96, 16, v226
	v_and_b32_e32 v97, 0xffff0000, v226
	v_add_f32_e32 v226, v92, v12
	v_add_f32_e32 v92, v93, v13
	v_add_f32_e32 v224, 1.0, v110
	v_add_f32_e32 v225, 1.0, v111
	v_mul_f32_e32 v226, 0xbfb8aa3b, v226
	v_mul_f32_e32 v92, 0xbfb8aa3b, v92
	v_rcp_f32_e32 v224, v224
	v_rcp_f32_e32 v225, v225
	v_exp_f32_e32 v226, v226
	v_exp_f32_e32 v110, v92
	v_lshlrev_b32_e32 v108, 16, v122
	v_and_b32_e32 v109, 0xffff0000, v122
	v_pk_fma_f32 v[92:93], v[224:225], v[96:97], v[108:109]
	v_add_f32_e32 v224, 1.0, v226
	v_add_f32_e32 v225, 1.0, v110
	v_rcp_f32_e32 v224, v224
	v_rcp_f32_e32 v225, v225
	v_add_f32_e32 v86, v86, v6
	v_add_f32_e32 v87, v87, v7
	v_lshlrev_b32_e32 v226, 16, v227
	v_and_b32_e32 v227, 0xffff0000, v227
	v_lshlrev_b32_e32 v96, 16, v123
	v_and_b32_e32 v97, 0xffff0000, v123
	v_mul_f32_e32 v86, 0xbfb8aa3b, v86
	v_mul_f32_e32 v87, 0xbfb8aa3b, v87
	v_pk_fma_f32 v[96:97], v[224:225], v[226:227], v[96:97]
	v_exp_f32_e32 v86, v86
	v_exp_f32_e32 v87, v87
	v_cvt_pk_bf16_f32 v224, v94, v95
	v_cvt_pk_bf16_f32 v225, v90, v91
	v_cvt_pk_bf16_f32 v226, v92, v93
	v_cvt_pk_bf16_f32 v227, v96, v97
	v_lshl_add_u64 v[90:91], v[120:121], 0, v[0:1]
	global_store_dwordx4 v[90:91], v[224:227], off
	v_add_f32_e32 v82, v82, v2
	v_add_f32_e32 v83, v83, v3
	s_waitcnt vmcnt(9)
	v_lshlrev_b32_e32 v226, 16, v228
	v_and_b32_e32 v227, 0xffff0000, v228
	v_add_f32_e32 v228, v88, v8
	v_mul_f32_e32 v228, 0xbfb8aa3b, v228
	v_add_f32_e32 v88, v89, v9
	v_add_f32_e32 v224, 1.0, v86
	v_add_f32_e32 v225, 1.0, v87
	v_exp_f32_e32 v228, v228
	v_mul_f32_e32 v88, 0xbfb8aa3b, v88
	v_rcp_f32_e32 v224, v224
	v_rcp_f32_e32 v225, v225
	v_exp_f32_e32 v88, v88
	v_lshlrev_b32_e32 v86, 16, v118
	v_and_b32_e32 v87, 0xffff0000, v118
	v_add_f32_e32 v228, 1.0, v228
	v_pk_fma_f32 v[224:225], v[224:225], v[226:227], v[86:87]
	v_rcp_f32_e32 v226, v228
	v_add_f32_e32 v228, 1.0, v88
	v_mul_f32_e32 v82, 0xbfb8aa3b, v82
	v_mul_f32_e32 v83, 0xbfb8aa3b, v83
	v_rcp_f32_e32 v227, v228
	v_exp_f32_e32 v82, v82
	v_exp_f32_e32 v83, v83
	v_lshlrev_b32_e32 v228, 16, v229
	v_and_b32_e32 v229, 0xffff0000, v229
	v_lshlrev_b32_e32 v86, 16, v119
	v_and_b32_e32 v87, 0xffff0000, v119
	v_pk_fma_f32 v[226:227], v[226:227], v[228:229], v[86:87]
	v_add_f32_e32 v228, 1.0, v82
	v_add_f32_e32 v229, 1.0, v83
	v_lshlrev_b32_e32 v82, 16, v230
	v_and_b32_e32 v83, 0xffff0000, v230
	v_add_f32_e32 v230, v84, v4
	v_add_f32_e32 v84, v85, v5
	v_mul_f32_e32 v230, 0xbfb8aa3b, v230
	v_mul_f32_e32 v84, 0xbfb8aa3b, v84
	v_rcp_f32_e32 v228, v228
	v_rcp_f32_e32 v229, v229
	v_exp_f32_e32 v230, v230
	v_exp_f32_e32 v84, v84
	v_lshlrev_b32_e32 v86, 16, v116
	v_and_b32_e32 v87, 0xffff0000, v116
	v_pk_fma_f32 v[82:83], v[228:229], v[82:83], v[86:87]
	v_add_f32_e32 v228, 1.0, v230
	v_add_f32_e32 v229, 1.0, v84
	v_rcp_f32_e32 v228, v228
	v_rcp_f32_e32 v229, v229
	v_lshlrev_b32_e32 v230, 16, v231
	v_and_b32_e32 v231, 0xffff0000, v231
	v_lshlrev_b32_e32 v84, 16, v117
	v_and_b32_e32 v85, 0xffff0000, v117
	v_pk_fma_f32 v[84:85], v[228:229], v[230:231], v[84:85]
	v_cvt_pk_bf16_f32 v228, v224, v225
	v_cvt_pk_bf16_f32 v229, v226, v227
	v_cvt_pk_bf16_f32 v230, v82, v83
	v_cvt_pk_bf16_f32 v231, v84, v85
	global_store_dwordx4 v[90:91], v[228:231], off offset:256
	v_mov_b32_e32 v84, 0
	s_and_b64 vcc, exec, s[0:1]
	v_or_b32_e32 v24, 32, v114
	v_mov_b64_e32 v[22:23], s[12:13]
	v_mad_i64_i32 v[22:23], s[28:29], v24, s66, v[22:23]
	v_lshl_add_u64 v[22:23], s[26:27], 1, v[22:23]
	v_lshl_add_u64 v[22:23], v[22:23], 0, v[0:1]
	v_ashrrev_i32_e32 v25, 31, v24
	v_lshlrev_b64 v[24:25], 11, v[24:25]
	v_lshl_add_u64 v[86:87], s[10:11], 0, v[24:25]
	v_mov_b32_e32 v90, 0
	v_mov_b32_e32 v91, 0
	v_mov_b32_e32 v88, 0
	v_mov_b32_e32 v89, 0
	s_cbranch_vccnz .LBB0_828
	v_lshl_add_u64 v[24:25], v[86:87], 0, v[0:1]
	global_load_dwordx2 v[90:91], v[24:25], off sc1
	global_load_dwordx2 v[88:89], v[24:25], off offset:8 sc1
.LBB0_828:
	s_nop 0
	s_and_b64 vcc, exec, s[0:1]
	v_mov_b32_e32 v85, 0
	v_mov_b32_e32 v82, 0
	v_mov_b32_e32 v83, 0
	s_cbranch_vccnz .LBB0_830
	v_lshl_add_u64 v[82:83], v[86:87], 0, v[0:1]
	global_load_dwordx2 v[84:85], v[82:83], off offset:256 sc1
	s_nop 0
	global_load_dwordx2 v[82:83], v[82:83], off offset:264 sc1
.LBB0_830:
	v_add_f32_e32 v78, v78, v14
	v_add_f32_e32 v79, v79, v15
	v_mul_f32_e32 v78, 0xbfb8aa3b, v78
	v_mul_f32_e32 v79, 0xbfb8aa3b, v79
	v_exp_f32_e32 v78, v78
	v_exp_f32_e32 v79, v79
	s_waitcnt vmcnt(9)
	v_lshlrev_b32_e32 v92, 16, v232
	v_and_b32_e32 v93, 0xffff0000, v232
	v_add_f32_e32 v232, v80, v16
	v_mul_f32_e32 v232, 0xbfb8aa3b, v232
	v_add_f32_e32 v80, v81, v17
	v_add_f32_e32 v78, 1.0, v78
	v_add_f32_e32 v79, 1.0, v79
	v_exp_f32_e32 v232, v232
	v_mul_f32_e32 v80, 0xbfb8aa3b, v80
	v_rcp_f32_e32 v78, v78
	v_rcp_f32_e32 v79, v79
	v_exp_f32_e32 v81, v80
	v_add_f32_e32 v74, v74, v10
	v_lshlrev_b32_e32 v94, 16, v106
	v_and_b32_e32 v95, 0xffff0000, v106
	v_add_f32_e32 v232, 1.0, v232
	v_mul_f32_e32 v74, 0xbfb8aa3b, v74
	v_pk_fma_f32 v[78:79], v[78:79], v[92:93], v[94:95]
	v_rcp_f32_e32 v80, v232
	v_add_f32_e32 v232, 1.0, v81
	v_exp_f32_e32 v94, v74
	v_add_f32_e32 v74, v75, v11
	v_rcp_f32_e32 v81, v232
	v_mul_f32_e32 v74, 0xbfb8aa3b, v74
	v_exp_f32_e32 v95, v74
	v_lshlrev_b32_e32 v232, 16, v233
	v_and_b32_e32 v233, 0xffff0000, v233
	v_lshlrev_b32_e32 v92, 16, v107
	v_and_b32_e32 v93, 0xffff0000, v107
	v_pk_fma_f32 v[74:75], v[80:81], v[232:233], v[92:93]
	v_lshlrev_b32_e32 v80, 16, v234
	v_and_b32_e32 v81, 0xffff0000, v234
	v_add_f32_e32 v234, v76, v12
	v_add_f32_e32 v76, v77, v13
	v_add_f32_e32 v232, 1.0, v94
	v_add_f32_e32 v233, 1.0, v95
	v_mul_f32_e32 v234, 0xbfb8aa3b, v234
	v_mul_f32_e32 v76, 0xbfb8aa3b, v76
	v_rcp_f32_e32 v232, v232
	v_rcp_f32_e32 v233, v233
	v_exp_f32_e32 v234, v234
	v_exp_f32_e32 v94, v76
	v_lshlrev_b32_e32 v92, 16, v104
	v_and_b32_e32 v93, 0xffff0000, v104
	v_pk_fma_f32 v[76:77], v[232:233], v[80:81], v[92:93]
	v_add_f32_e32 v232, 1.0, v234
	v_add_f32_e32 v233, 1.0, v94
	v_rcp_f32_e32 v232, v232
	v_rcp_f32_e32 v233, v233
	v_add_f32_e32 v70, v70, v6
	v_add_f32_e32 v71, v71, v7
	v_lshlrev_b32_e32 v234, 16, v235
	v_and_b32_e32 v235, 0xffff0000, v235
	v_lshlrev_b32_e32 v80, 16, v105
	v_and_b32_e32 v81, 0xffff0000, v105
	v_mul_f32_e32 v70, 0xbfb8aa3b, v70
	v_mul_f32_e32 v71, 0xbfb8aa3b, v71
	v_pk_fma_f32 v[80:81], v[232:233], v[234:235], v[80:81]
	v_exp_f32_e32 v70, v70
	v_exp_f32_e32 v71, v71
	v_cvt_pk_bf16_f32 v232, v78, v79
	v_cvt_pk_bf16_f32 v233, v74, v75
	v_cvt_pk_bf16_f32 v234, v76, v77
	v_cvt_pk_bf16_f32 v235, v80, v81
	v_lshl_add_u64 v[74:75], v[102:103], 0, v[0:1]
	global_store_dwordx4 v[74:75], v[232:235], off
	v_add_f32_e32 v66, v66, v2
	v_add_f32_e32 v67, v67, v3
	s_waitcnt vmcnt(7)
	v_lshlrev_b32_e32 v234, 16, v236
	v_and_b32_e32 v235, 0xffff0000, v236
	v_add_f32_e32 v236, v72, v8
	v_mul_f32_e32 v236, 0xbfb8aa3b, v236
	v_add_f32_e32 v72, v73, v9
	v_add_f32_e32 v232, 1.0, v70
	v_add_f32_e32 v233, 1.0, v71
	v_exp_f32_e32 v236, v236
	v_mul_f32_e32 v72, 0xbfb8aa3b, v72
	v_rcp_f32_e32 v232, v232
	v_rcp_f32_e32 v233, v233
	v_exp_f32_e32 v72, v72
	v_lshlrev_b32_e32 v70, 16, v100
	v_and_b32_e32 v71, 0xffff0000, v100
	v_add_f32_e32 v236, 1.0, v236
	v_pk_fma_f32 v[232:233], v[232:233], v[234:235], v[70:71]
	v_rcp_f32_e32 v234, v236
	v_add_f32_e32 v236, 1.0, v72
	v_mul_f32_e32 v66, 0xbfb8aa3b, v66
	v_mul_f32_e32 v67, 0xbfb8aa3b, v67
	v_rcp_f32_e32 v235, v236
	v_exp_f32_e32 v66, v66
	v_exp_f32_e32 v67, v67
	v_lshlrev_b32_e32 v236, 16, v237
	v_and_b32_e32 v237, 0xffff0000, v237
	v_lshlrev_b32_e32 v70, 16, v101
	v_and_b32_e32 v71, 0xffff0000, v101
	v_pk_fma_f32 v[234:235], v[234:235], v[236:237], v[70:71]
	v_add_f32_e32 v236, 1.0, v66
	v_add_f32_e32 v237, 1.0, v67
	v_lshlrev_b32_e32 v66, 16, v238
	v_and_b32_e32 v67, 0xffff0000, v238
	v_add_f32_e32 v238, v68, v4
	v_add_f32_e32 v68, v69, v5
	v_mul_f32_e32 v238, 0xbfb8aa3b, v238
	v_mul_f32_e32 v68, 0xbfb8aa3b, v68
	v_rcp_f32_e32 v236, v236
	v_rcp_f32_e32 v237, v237
	v_exp_f32_e32 v238, v238
	v_exp_f32_e32 v68, v68
	v_lshlrev_b32_e32 v70, 16, v98
	v_and_b32_e32 v71, 0xffff0000, v98
	v_pk_fma_f32 v[66:67], v[236:237], v[66:67], v[70:71]
	v_add_f32_e32 v236, 1.0, v238
	v_add_f32_e32 v237, 1.0, v68
	v_rcp_f32_e32 v236, v236
	v_rcp_f32_e32 v237, v237
	v_lshlrev_b32_e32 v238, 16, v239
	v_and_b32_e32 v239, 0xffff0000, v239
	v_lshlrev_b32_e32 v68, 16, v99
	v_and_b32_e32 v69, 0xffff0000, v99
	v_pk_fma_f32 v[68:69], v[236:237], v[238:239], v[68:69]
	v_cvt_pk_bf16_f32 v236, v232, v233
	v_cvt_pk_bf16_f32 v237, v234, v235
	v_cvt_pk_bf16_f32 v238, v66, v67
	v_cvt_pk_bf16_f32 v239, v68, v69
	global_store_dwordx4 v[74:75], v[236:239], off offset:256
	v_mov_b32_e32 v68, 0
	s_and_b64 vcc, exec, s[0:1]
	v_or_b32_e32 v20, 48, v114
	v_mov_b64_e32 v[18:19], s[12:13]
	v_mad_i64_i32 v[18:19], s[28:29], v20, s66, v[18:19]
	v_lshl_add_u64 v[18:19], s[26:27], 1, v[18:19]
	v_lshl_add_u64 v[18:19], v[18:19], 0, v[0:1]
	v_ashrrev_i32_e32 v21, 31, v20
	v_lshlrev_b64 v[20:21], 11, v[20:21]
	v_lshl_add_u64 v[70:71], s[10:11], 0, v[20:21]
	v_mov_b32_e32 v74, 0
	v_mov_b32_e32 v75, 0
	v_mov_b32_e32 v72, 0
	v_mov_b32_e32 v73, 0
	s_cbranch_vccnz .LBB0_832
	v_lshl_add_u64 v[20:21], v[70:71], 0, v[0:1]
	global_load_dwordx2 v[74:75], v[20:21], off sc1
	global_load_dwordx2 v[72:73], v[20:21], off offset:8 sc1
.LBB0_832:
	s_nop 0
	s_and_b64 vcc, exec, s[0:1]
	v_mov_b32_e32 v69, 0
	v_mov_b32_e32 v66, 0
	v_mov_b32_e32 v67, 0
	s_cbranch_vccnz .LBB0_834
	v_lshl_add_u64 v[66:67], v[70:71], 0, v[0:1]
	global_load_dwordx2 v[68:69], v[66:67], off offset:256 sc1
	s_nop 0
	global_load_dwordx2 v[66:67], v[66:67], off offset:264 sc1
.LBB0_834:
	v_add_f32_e32 v62, v62, v14
	v_add_f32_e32 v63, v63, v15
	v_mul_f32_e32 v62, 0xbfb8aa3b, v62
	v_mul_f32_e32 v63, 0xbfb8aa3b, v63
	v_exp_f32_e32 v62, v62
	v_exp_f32_e32 v63, v63
	s_waitcnt vmcnt(8)
	v_lshlrev_b32_e32 v76, 16, v198
	v_and_b32_e32 v77, 0xffff0000, v198
	v_add_f32_e32 v198, v64, v16
	v_mul_f32_e32 v198, 0xbfb8aa3b, v198
	v_add_f32_e32 v64, v65, v17
	v_add_f32_e32 v62, 1.0, v62
	v_add_f32_e32 v63, 1.0, v63
	v_exp_f32_e32 v198, v198
	v_mul_f32_e32 v64, 0xbfb8aa3b, v64
	v_rcp_f32_e32 v62, v62
	v_rcp_f32_e32 v63, v63
	v_exp_f32_e32 v65, v64
	v_add_f32_e32 v58, v58, v10
	v_lshlrev_b32_e32 v78, 16, v90
	v_and_b32_e32 v79, 0xffff0000, v90
	v_add_f32_e32 v198, 1.0, v198
	v_mul_f32_e32 v58, 0xbfb8aa3b, v58
	v_pk_fma_f32 v[62:63], v[62:63], v[76:77], v[78:79]
	v_rcp_f32_e32 v64, v198
	v_add_f32_e32 v198, 1.0, v65
	v_exp_f32_e32 v78, v58
	v_add_f32_e32 v58, v59, v11
	v_rcp_f32_e32 v65, v198
	v_mul_f32_e32 v58, 0xbfb8aa3b, v58
	v_exp_f32_e32 v79, v58
	v_lshlrev_b32_e32 v198, 16, v199
	v_and_b32_e32 v199, 0xffff0000, v199
	v_lshlrev_b32_e32 v76, 16, v91
	v_and_b32_e32 v77, 0xffff0000, v91
	v_pk_fma_f32 v[58:59], v[64:65], v[198:199], v[76:77]
	v_lshlrev_b32_e32 v64, 16, v200
	v_and_b32_e32 v65, 0xffff0000, v200
	v_add_f32_e32 v200, v60, v12
	v_add_f32_e32 v60, v61, v13
	v_add_f32_e32 v198, 1.0, v78
	v_add_f32_e32 v199, 1.0, v79
	v_mul_f32_e32 v200, 0xbfb8aa3b, v200
	v_mul_f32_e32 v60, 0xbfb8aa3b, v60
	v_rcp_f32_e32 v198, v198
	v_rcp_f32_e32 v199, v199
	v_exp_f32_e32 v200, v200
	v_exp_f32_e32 v78, v60
	v_lshlrev_b32_e32 v76, 16, v88
	v_and_b32_e32 v77, 0xffff0000, v88
	v_pk_fma_f32 v[60:61], v[198:199], v[64:65], v[76:77]
	v_add_f32_e32 v198, 1.0, v200
	v_add_f32_e32 v199, 1.0, v78
	v_rcp_f32_e32 v198, v198
	v_rcp_f32_e32 v199, v199
	v_add_f32_e32 v54, v54, v6
	v_add_f32_e32 v55, v55, v7
	v_lshlrev_b32_e32 v200, 16, v201
	v_and_b32_e32 v201, 0xffff0000, v201
	v_lshlrev_b32_e32 v64, 16, v89
	v_and_b32_e32 v65, 0xffff0000, v89
	v_mul_f32_e32 v54, 0xbfb8aa3b, v54
	v_mul_f32_e32 v55, 0xbfb8aa3b, v55
	v_pk_fma_f32 v[64:65], v[198:199], v[200:201], v[64:65]
	v_exp_f32_e32 v54, v54
	v_exp_f32_e32 v55, v55
	v_cvt_pk_bf16_f32 v198, v62, v63
	v_cvt_pk_bf16_f32 v199, v58, v59
	v_cvt_pk_bf16_f32 v200, v60, v61
	v_cvt_pk_bf16_f32 v201, v64, v65
	v_lshl_add_u64 v[58:59], v[86:87], 0, v[0:1]
	global_store_dwordx4 v[58:59], v[198:201], off
	v_add_f32_e32 v50, v50, v2
	v_add_f32_e32 v51, v51, v3
	s_waitcnt vmcnt(7)
	v_lshlrev_b32_e32 v200, 16, v202
	v_and_b32_e32 v201, 0xffff0000, v202
	v_add_f32_e32 v202, v56, v8
	v_mul_f32_e32 v202, 0xbfb8aa3b, v202
	v_add_f32_e32 v56, v57, v9
	v_add_f32_e32 v198, 1.0, v54
	v_add_f32_e32 v199, 1.0, v55
	v_exp_f32_e32 v202, v202
	v_mul_f32_e32 v56, 0xbfb8aa3b, v56
	v_rcp_f32_e32 v198, v198
	v_rcp_f32_e32 v199, v199
	v_exp_f32_e32 v56, v56
	v_lshlrev_b32_e32 v54, 16, v84
	v_and_b32_e32 v55, 0xffff0000, v84
	v_add_f32_e32 v202, 1.0, v202
	v_pk_fma_f32 v[198:199], v[198:199], v[200:201], v[54:55]
	v_rcp_f32_e32 v200, v202
	v_add_f32_e32 v202, 1.0, v56
	v_mul_f32_e32 v50, 0xbfb8aa3b, v50
	v_mul_f32_e32 v51, 0xbfb8aa3b, v51
	v_rcp_f32_e32 v201, v202
	v_exp_f32_e32 v50, v50
	v_exp_f32_e32 v51, v51
	v_lshlrev_b32_e32 v202, 16, v203
	v_and_b32_e32 v203, 0xffff0000, v203
	v_lshlrev_b32_e32 v54, 16, v85
	v_and_b32_e32 v55, 0xffff0000, v85
	v_pk_fma_f32 v[200:201], v[200:201], v[202:203], v[54:55]
	v_add_f32_e32 v202, 1.0, v50
	v_add_f32_e32 v203, 1.0, v51
	v_lshlrev_b32_e32 v50, 16, v204
	v_and_b32_e32 v51, 0xffff0000, v204
	v_add_f32_e32 v204, v52, v4
	v_add_f32_e32 v52, v53, v5
	v_mul_f32_e32 v204, 0xbfb8aa3b, v204
	v_mul_f32_e32 v52, 0xbfb8aa3b, v52
	v_rcp_f32_e32 v202, v202
	v_rcp_f32_e32 v203, v203
	v_exp_f32_e32 v204, v204
	v_exp_f32_e32 v52, v52
	v_add_f32_e32 v14, v46, v14
	v_add_f32_e32 v15, v47, v15
	v_lshlrev_b32_e32 v54, 16, v82
	v_and_b32_e32 v55, 0xffff0000, v82
	v_mul_f32_e32 v14, 0xbfb8aa3b, v14
	v_mul_f32_e32 v15, 0xbfb8aa3b, v15
	v_pk_fma_f32 v[50:51], v[202:203], v[50:51], v[54:55]
	v_add_f32_e32 v202, 1.0, v204
	v_add_f32_e32 v203, 1.0, v52
	v_exp_f32_e32 v14, v14
	v_exp_f32_e32 v15, v15
	v_rcp_f32_e32 v202, v202
	v_rcp_f32_e32 v203, v203
	v_add_f32_e32 v16, v48, v16
	v_add_f32_e32 v17, v49, v17
	v_mul_f32_e32 v16, 0xbfb8aa3b, v16
	v_mul_f32_e32 v17, 0xbfb8aa3b, v17
	v_add_f32_e32 v10, v42, v10
	v_add_f32_e32 v11, v43, v11
	v_exp_f32_e32 v16, v16
	v_exp_f32_e32 v17, v17
	v_mul_f32_e32 v10, 0xbfb8aa3b, v10
	v_mul_f32_e32 v11, 0xbfb8aa3b, v11
	v_lshlrev_b32_e32 v204, 16, v205
	v_and_b32_e32 v205, 0xffff0000, v205
	v_lshlrev_b32_e32 v52, 16, v83
	v_and_b32_e32 v53, 0xffff0000, v83
	v_add_f32_e32 v14, 1.0, v14
	v_add_f32_e32 v15, 1.0, v15
	v_exp_f32_e32 v10, v10
	v_exp_f32_e32 v11, v11
	v_pk_fma_f32 v[52:53], v[202:203], v[204:205], v[52:53]
	v_rcp_f32_e32 v14, v14
	v_rcp_f32_e32 v15, v15
	v_add_f32_e32 v12, v44, v12
	v_cvt_pk_bf16_f32 v202, v198, v199
	v_cvt_pk_bf16_f32 v203, v200, v201
	v_cvt_pk_bf16_f32 v204, v50, v51
	v_cvt_pk_bf16_f32 v205, v52, v53
	v_mul_f32_e32 v12, 0xbfb8aa3b, v12
	global_store_dwordx4 v[58:59], v[202:205], off offset:256
	v_add_f32_e32 v16, 1.0, v16
	v_add_f32_e32 v17, 1.0, v17
	s_waitcnt vmcnt(4)
	v_lshlrev_b32_e32 v22, 16, v206
	v_and_b32_e32 v23, 0xffff0000, v206
	v_exp_f32_e32 v206, v12
	v_add_f32_e32 v12, v45, v13
	v_lshlrev_b32_e32 v24, 16, v74
	v_and_b32_e32 v25, 0xffff0000, v74
	v_rcp_f32_e32 v16, v16
	v_rcp_f32_e32 v17, v17
	v_add_f32_e32 v10, 1.0, v10
	v_add_f32_e32 v11, 1.0, v11
	v_mul_f32_e32 v12, 0xbfb8aa3b, v12
	v_pk_fma_f32 v[14:15], v[14:15], v[22:23], v[24:25]
	v_lshlrev_b32_e32 v22, 16, v207
	v_and_b32_e32 v23, 0xffff0000, v207
	v_rcp_f32_e32 v10, v10
	v_rcp_f32_e32 v11, v11
	v_exp_f32_e32 v207, v12
	v_lshlrev_b32_e32 v24, 16, v75
	v_and_b32_e32 v25, 0xffff0000, v75
	v_pk_fma_f32 v[16:17], v[16:17], v[22:23], v[24:25]
	v_lshlrev_b32_e32 v22, 16, v208
	v_and_b32_e32 v23, 0xffff0000, v208
	v_lshlrev_b32_e32 v24, 16, v72
	v_and_b32_e32 v25, 0xffff0000, v72
	v_pk_fma_f32 v[12:13], v[10:11], v[22:23], v[24:25]
	v_add_f32_e32 v10, 1.0, v206
	v_add_f32_e32 v11, 1.0, v207
	v_rcp_f32_e32 v10, v10
	v_rcp_f32_e32 v11, v11
	v_lshlrev_b32_e32 v22, 16, v209
	v_and_b32_e32 v23, 0xffff0000, v209
	v_lshlrev_b32_e32 v24, 16, v73
	v_and_b32_e32 v25, 0xffff0000, v73
	v_pk_fma_f32 v[22:23], v[10:11], v[22:23], v[24:25]
	v_cvt_pk_bf16_f32 v10, v14, v15
	v_lshl_add_u64 v[14:15], v[70:71], 0, v[0:1]
	v_add_f32_e32 v0, v38, v6
	v_mul_f32_e32 v0, 0xbfb8aa3b, v0
	v_add_f32_e32 v6, v39, v7
	v_exp_f32_e32 v0, v0
	v_mul_f32_e32 v6, 0xbfb8aa3b, v6
	v_exp_f32_e32 v7, v6
	v_cvt_pk_bf16_f32 v11, v16, v17
	v_add_f32_e32 v0, 1.0, v0
	v_rcp_f32_e32 v6, v0
	v_add_f32_e32 v0, 1.0, v7
	v_rcp_f32_e32 v7, v0
	v_add_f32_e32 v0, v40, v8
	v_mul_f32_e32 v0, 0xbfb8aa3b, v0
	v_add_f32_e32 v8, v41, v9
	v_exp_f32_e32 v0, v0
	v_mul_f32_e32 v8, 0xbfb8aa3b, v8
	v_exp_f32_e32 v9, v8
	v_cvt_pk_bf16_f32 v12, v12, v13
	v_add_f32_e32 v0, 1.0, v0
	v_rcp_f32_e32 v8, v0
	v_add_f32_e32 v0, 1.0, v9
	v_rcp_f32_e32 v9, v0
	v_add_f32_e32 v0, v34, v2
	v_mul_f32_e32 v0, 0xbfb8aa3b, v0
	v_add_f32_e32 v2, v35, v3
	v_exp_f32_e32 v0, v0
	v_mul_f32_e32 v2, 0xbfb8aa3b, v2
	v_exp_f32_e32 v3, v2
	v_cvt_pk_bf16_f32 v13, v22, v23
	v_add_f32_e32 v0, 1.0, v0
	v_rcp_f32_e32 v2, v0
	v_add_f32_e32 v0, 1.0, v3
	v_rcp_f32_e32 v3, v0
	v_add_f32_e32 v0, v36, v4
	v_mul_f32_e32 v0, 0xbfb8aa3b, v0
	v_add_f32_e32 v4, v37, v5
	v_exp_f32_e32 v0, v0
	v_mul_f32_e32 v4, 0xbfb8aa3b, v4
	v_exp_f32_e32 v16, v4
	global_store_dwordx4 v[14:15], v[10:13], off
	v_add_f32_e32 v0, 1.0, v0
	s_andn2_b64 vcc, exec, s[38:39]
	s_waitcnt vmcnt(3)
	v_lshlrev_b32_e32 v10, 16, v216
	v_and_b32_e32 v11, 0xffff0000, v216
	v_lshlrev_b32_e32 v12, 16, v68
	v_and_b32_e32 v13, 0xffff0000, v68
	v_pk_fma_f32 v[6:7], v[6:7], v[10:11], v[12:13]
	v_lshlrev_b32_e32 v10, 16, v217
	v_and_b32_e32 v11, 0xffff0000, v217
	v_lshlrev_b32_e32 v12, 16, v69
	v_and_b32_e32 v13, 0xffff0000, v69
	v_pk_fma_f32 v[8:9], v[8:9], v[10:11], v[12:13]
	v_lshlrev_b32_e32 v10, 16, v218
	v_and_b32_e32 v11, 0xffff0000, v218
	v_lshlrev_b32_e32 v12, 16, v66
	v_and_b32_e32 v13, 0xffff0000, v66
	v_pk_fma_f32 v[4:5], v[2:3], v[10:11], v[12:13]
	v_rcp_f32_e32 v2, v0
	v_add_f32_e32 v0, 1.0, v16
	v_rcp_f32_e32 v3, v0
	v_lshlrev_b32_e32 v10, 16, v219
	v_and_b32_e32 v11, 0xffff0000, v219
	v_lshlrev_b32_e32 v12, 16, v67
	v_and_b32_e32 v13, 0xffff0000, v67
	v_pk_fma_f32 v[10:11], v[2:3], v[10:11], v[12:13]
	v_cvt_pk_bf16_f32 v2, v6, v7
	v_cvt_pk_bf16_f32 v3, v8, v9
	v_cvt_pk_bf16_f32 v4, v4, v5
	v_cvt_pk_bf16_f32 v5, v10, v11
	s_mov_b64 s[0:1], -1
	global_store_dwordx4 v[14:15], v[2:5], off offset:256
	s_cbranch_vccnz .LBB0_795
	v_readlane_b32 s28, v253, 4
	v_readlane_b32 s30, v253, 6
	v_readlane_b32 s31, v253, 7
	v_readlane_b32 s29, v253, 5
	s_and_b64 vcc, exec, s[8:9]
	v_mov_b64_e32 v[36:37], s[30:31]
	v_mov_b64_e32 v[160:161], s[30:31]
	v_mov_b64_e32 v[156:157], s[30:31]
	v_mov_b64_e32 v[144:145], s[30:31]
	v_mov_b64_e32 v[140:141], s[30:31]
	v_mov_b64_e32 v[128:129], s[30:31]
	v_mov_b64_e32 v[124:125], s[30:31]
	v_mov_b64_e32 v[112:113], s[30:31]
	v_mov_b64_e32 v[108:109], s[30:31]
	v_mov_b64_e32 v[152:153], s[30:31]
	v_mov_b64_e32 v[148:149], s[30:31]
	v_mov_b64_e32 v[136:137], s[30:31]
	v_mov_b64_e32 v[132:133], s[30:31]
	v_mov_b64_e32 v[120:121], s[30:31]
	v_mov_b64_e32 v[116:117], s[30:31]
	v_mov_b64_e32 v[104:105], s[30:31]
	v_mov_b64_e32 v[100:101], s[30:31]
	v_mov_b64_e32 v[96:97], s[30:31]
	v_mov_b64_e32 v[92:93], s[30:31]
	v_mov_b64_e32 v[80:81], s[30:31]
	v_mov_b64_e32 v[76:77], s[30:31]
	v_mov_b64_e32 v[64:65], s[30:31]
	v_mov_b64_e32 v[60:61], s[30:31]
	v_mov_b64_e32 v[48:49], s[30:31]
	v_mov_b64_e32 v[44:45], s[30:31]
	v_mov_b64_e32 v[88:89], s[30:31]
	v_mov_b64_e32 v[84:85], s[30:31]
	v_mov_b64_e32 v[72:73], s[30:31]
	v_mov_b64_e32 v[68:69], s[30:31]
	v_mov_b64_e32 v[56:57], s[30:31]
	v_mov_b64_e32 v[52:53], s[30:31]
	v_mov_b64_e32 v[40:41], s[30:31]
	v_mov_b64_e32 v[34:35], s[28:29]
	v_mov_b64_e32 v[158:159], s[28:29]
	v_mov_b64_e32 v[154:155], s[28:29]
	v_mov_b64_e32 v[142:143], s[28:29]
	v_mov_b64_e32 v[138:139], s[28:29]
	v_mov_b64_e32 v[126:127], s[28:29]
	v_mov_b64_e32 v[122:123], s[28:29]
	v_mov_b64_e32 v[110:111], s[28:29]
	v_mov_b64_e32 v[106:107], s[28:29]
	v_mov_b64_e32 v[150:151], s[28:29]
	v_mov_b64_e32 v[146:147], s[28:29]
	v_mov_b64_e32 v[134:135], s[28:29]
	v_mov_b64_e32 v[130:131], s[28:29]
	v_mov_b64_e32 v[118:119], s[28:29]
	v_mov_b64_e32 v[114:115], s[28:29]
	v_mov_b64_e32 v[102:103], s[28:29]
	v_mov_b64_e32 v[98:99], s[28:29]
	v_mov_b64_e32 v[94:95], s[28:29]
	v_mov_b64_e32 v[90:91], s[28:29]
	v_mov_b64_e32 v[78:79], s[28:29]
	v_mov_b64_e32 v[74:75], s[28:29]
	v_mov_b64_e32 v[62:63], s[28:29]
	v_mov_b64_e32 v[58:59], s[28:29]
	v_mov_b64_e32 v[46:47], s[28:29]
	v_mov_b64_e32 v[42:43], s[28:29]
	v_mov_b64_e32 v[86:87], s[28:29]
	v_mov_b64_e32 v[82:83], s[28:29]
	v_mov_b64_e32 v[70:71], s[28:29]
	v_mov_b64_e32 v[66:67], s[28:29]
	v_mov_b64_e32 v[54:55], s[28:29]
	v_mov_b64_e32 v[50:51], s[28:29]
	v_mov_b64_e32 v[38:39], s[28:29]
	s_cbranch_vccz .LBB0_794
	s_barrier
	s_branch .LBB0_794
